# expert token-count loads of moe_tables and gather zero-fill issued together instead of one serialized round trip each
# baseline (speedup 1.0000x reference)
; #define LAS __attribute__((address_space(3)))
; __device__ __forceinline__ int moe_tables(Frame& F) {
;     LAS int* seg = (LAS int*)(F.lds + MISC_OFF + 1024); LAS int* tile_e = (LAS int*)(F.lds + MISC_OFF + 64);
;     if (F.tid == 0) { int s = 0;
;         for (int e = 0; e < 8; ++e) { seg[e] = s; const int c = (int)__hip_atomic_load(F.ctl + CW_CNT + 64 * e, RLX_AGENT); const int nt = (c + 255) >> 8; for (int i = 0; i < nt; ++i) tile_e[(s >> 8) + i] = e; s += nt << 8; }
;         seg[8] = s; }
;     __syncthreads();
.LBB0_1595:
	s_cmp_lt_i32 s68, 16
	s_cselect_b64 s[2:3], -1, 0
	s_add_u32 s8, s86, 0x5f800000
	s_addc_u32 s9, s87, 0
	s_and_b64 s[4:5], s[2:3], s[0:1]
	s_andn2_b64 vcc, exec, s[4:5]
	s_cbranch_vccnz .LBB0_1725
	v_cmp_eq_u32_e32 vcc, 0, v0
	s_and_saveexec_b64 s[6:7], vcc
	s_cbranch_execz .LBB0_1694
	s_add_i32 s0, 0, 0x20400
	v_mov_b32_e32 v1, 0
	s_waitcnt vmcnt(0)
	v_mov_b32_e32 v2, s0
	ds_write_b32 v2, v1
	v_mov_b32_e32 v1, 0x8000
	global_load_dword v248, v1, s[86:87] sc1
	global_load_dword v249, v1, s[86:87] offset:256 sc1
	global_load_dword v250, v1, s[86:87] offset:512 sc1
	global_load_dword v251, v1, s[86:87] offset:768 sc1
	global_load_dword v252, v1, s[86:87] offset:1024 sc1
	global_load_dword v253, v1, s[86:87] offset:1280 sc1
	global_load_dword v254, v1, s[86:87] offset:1536 sc1
	global_load_dword v255, v1, s[86:87] offset:1792 sc1
	s_waitcnt vmcnt(0)
	v_mov_b32_e32 v2, v248
	s_nop 0
	v_readfirstlane_b32 s10, v2
	s_addk_i32 s10, 0xff
	s_ashr_i32 s11, s10, 8
	s_cmp_lt_i32 s11, 1
	s_cbranch_scc1 .LBB0_1609
	s_cmp_lt_u32 s11, 4
	s_cbranch_scc1 .LBB0_1606
	s_add_i32 s0, s11, -4
	s_lshr_b32 s12, s0, 2
	s_add_i32 s12, s12, 1
	s_cmp_lt_u32 s0, 28
	s_mov_b32 s0, 0
	s_cbranch_scc1 .LBB0_1602
	s_mov_b32 s2, s0
	s_mov_b32 s3, s0
	s_mov_b32 s1, s0
	v_mov_b64_e32 v[4:5], s[2:3]
	s_add_i32 s13, 0, 0x20040
	s_and_b32 s14, s12, 0x7ffffff8
	v_mov_b64_e32 v[2:3], s[0:1]

; __device__ __forceinline__ int moe_tables(Frame& F) {
;     ...
;         for (int e = 0; e < 8; ++e) { seg[e] = s; const int c = (int)__hip_atomic_load(F.ctl + CW_CNT + 64 * e, RLX_AGENT); const int nt = (c + 255) >> 8; for (int i = 0; i < nt; ++i) tile_e[(s >> 8) + i] = e; s += nt << 8; }
.LBB0_1609:
	s_and_b32 s2, s10, 0xffffff00
	s_add_i32 s0, 0, 0x20404
	v_mov_b32_e32 v2, s0
	v_mov_b32_e32 v3, s2
	ds_write_b32 v2, v3
	s_mov_b32 s12, 0
	s_waitcnt vmcnt(0)
	v_mov_b32_e32 v1, v249
	s_nop 0
	v_readfirstlane_b32 s3, v1
	s_addk_i32 s3, 0xff
	s_ashr_i32 s10, s3, 8
	s_cmp_lt_i32 s10, 1
	s_cbranch_scc1 .LBB0_1621
	s_ashr_i32 s11, s2, 6
	s_cmp_eq_u32 s10, 1
	s_mov_b64 s[0:1], -1
	s_cbranch_scc1 .LBB0_1618
	s_add_i32 s1, s10, -2
	s_lshr_b32 s0, s1, 1
	s_add_i32 s0, s0, 1
	s_cmp_lt_u32 s1, 14
	s_mov_b32 s1, 0
	s_cbranch_scc1 .LBB0_1614
	s_add_i32 s13, s11, 0
	s_and_b32 s12, s0, -8
	s_add_i32 s13, s13, 0x20040
	v_mov_b32_e32 v1, 1

; __device__ __forceinline__ int moe_tables(Frame& F) {
;     ...
;         for (int e = 0; e < 8; ++e) { seg[e] = s; const int c = (int)__hip_atomic_load(F.ctl + CW_CNT + 64 * e, RLX_AGENT); const int nt = (c + 255) >> 8; for (int i = 0; i < nt; ++i) tile_e[(s >> 8) + i] = e; s += nt << 8; }
.LBB0_1621:
	s_and_b32 s0, s3, 0xffffff00
	s_add_i32 s2, s0, s2
	s_add_i32 s0, 0, 0x20408
	v_mov_b32_e32 v1, s0
	v_mov_b32_e32 v2, s2
	ds_write_b32 v1, v2
	v_mov_b32_e32 v1, 0x8000
	s_waitcnt vmcnt(0)
	v_mov_b32_e32 v2, v250
	s_nop 0
	v_readfirstlane_b32 s3, v2
	s_addk_i32 s3, 0xff
	s_ashr_i32 s10, s3, 8
	s_cmp_lt_i32 s10, 1
	s_cbranch_scc1 .LBB0_1633
	s_ashr_i32 s11, s2, 6
	s_cmp_eq_u32 s10, 1
	s_cbranch_scc1 .LBB0_1630
	s_add_i32 s1, s10, -2
	s_lshr_b32 s0, s1, 1
	s_add_i32 s0, s0, 1
	s_cmp_lt_u32 s1, 14
	s_mov_b32 s1, 0
	s_cbranch_scc1 .LBB0_1626
	s_add_i32 s13, s11, 0
	s_and_b32 s12, s0, -8
	s_add_i32 s13, s13, 0x20040
	v_mov_b32_e32 v2, 2

; __device__ __forceinline__ int moe_tables(Frame& F) {
;     ...
;         for (int e = 0; e < 8; ++e) { seg[e] = s; const int c = (int)__hip_atomic_load(F.ctl + CW_CNT + 64 * e, RLX_AGENT); const int nt = (c + 255) >> 8; for (int i = 0; i < nt; ++i) tile_e[(s >> 8) + i] = e; s += nt << 8; }
.LBB0_1633:
	s_and_b32 s0, s3, 0xffffff00
	s_add_i32 s2, s0, s2
	s_add_i32 s0, 0, 0x2040c
	v_mov_b32_e32 v2, s0
	v_mov_b32_e32 v3, s2
	ds_write_b32 v2, v3
	s_mov_b32 s12, 0
	s_waitcnt vmcnt(0)
	v_mov_b32_e32 v1, v251
	s_nop 0
	v_readfirstlane_b32 s3, v1
	s_addk_i32 s3, 0xff
	s_ashr_i32 s10, s3, 8
	s_cmp_lt_i32 s10, 1
	s_cbranch_scc1 .LBB0_1645
	s_ashr_i32 s11, s2, 6
	s_cmp_eq_u32 s10, 1
	s_mov_b64 s[0:1], -1
	s_cbranch_scc1 .LBB0_1642
	s_add_i32 s1, s10, -2
	s_lshr_b32 s0, s1, 1
	s_add_i32 s0, s0, 1
	s_cmp_lt_u32 s1, 14
	s_mov_b32 s1, 0
	s_cbranch_scc1 .LBB0_1638
	s_add_i32 s13, s11, 0
	s_and_b32 s12, s0, -8
	s_add_i32 s13, s13, 0x20040
	v_mov_b32_e32 v1, 3

; __device__ __forceinline__ int moe_tables(Frame& F) {
;     ...
;         for (int e = 0; e < 8; ++e) { seg[e] = s; const int c = (int)__hip_atomic_load(F.ctl + CW_CNT + 64 * e, RLX_AGENT); const int nt = (c + 255) >> 8; for (int i = 0; i < nt; ++i) tile_e[(s >> 8) + i] = e; s += nt << 8; }
.LBB0_1645:
	s_and_b32 s0, s3, 0xffffff00
	s_add_i32 s2, s0, s2
	s_add_i32 s0, 0, 0x20410
	v_mov_b32_e32 v1, s0
	v_mov_b32_e32 v2, s2
	ds_write_b32 v1, v2
	v_mov_b32_e32 v1, 0x8000
	s_waitcnt vmcnt(0)
	v_mov_b32_e32 v2, v252
	s_nop 0
	v_readfirstlane_b32 s3, v2
	s_addk_i32 s3, 0xff
	s_ashr_i32 s10, s3, 8
	s_cmp_lt_i32 s10, 1
	s_cbranch_scc1 .LBB0_1657
	s_ashr_i32 s11, s2, 6
	s_cmp_eq_u32 s10, 1
	s_cbranch_scc1 .LBB0_1654
	s_add_i32 s1, s10, -2
	s_lshr_b32 s0, s1, 1
	s_add_i32 s0, s0, 1
	s_cmp_lt_u32 s1, 14
	s_mov_b32 s1, 0
	s_cbranch_scc1 .LBB0_1650
	s_add_i32 s13, s11, 0
	s_and_b32 s12, s0, -8
	s_add_i32 s13, s13, 0x20040
	v_mov_b32_e32 v2, 4

; __device__ __forceinline__ int moe_tables(Frame& F) {
;     ...
;         for (int e = 0; e < 8; ++e) { seg[e] = s; const int c = (int)__hip_atomic_load(F.ctl + CW_CNT + 64 * e, RLX_AGENT); const int nt = (c + 255) >> 8; for (int i = 0; i < nt; ++i) tile_e[(s >> 8) + i] = e; s += nt << 8; }
.LBB0_1657:
	s_and_b32 s0, s3, 0xffffff00
	s_add_i32 s2, s0, s2
	s_add_i32 s0, 0, 0x20414
	v_mov_b32_e32 v2, s0
	v_mov_b32_e32 v3, s2
	ds_write_b32 v2, v3
	s_mov_b32 s12, 0
	s_waitcnt vmcnt(0)
	v_mov_b32_e32 v1, v253
	s_nop 0
	v_readfirstlane_b32 s3, v1
	s_addk_i32 s3, 0xff
	s_ashr_i32 s10, s3, 8
	s_cmp_lt_i32 s10, 1
	s_cbranch_scc1 .LBB0_1669
	s_ashr_i32 s11, s2, 6
	s_cmp_eq_u32 s10, 1
	s_mov_b64 s[0:1], -1
	s_cbranch_scc1 .LBB0_1666
	s_add_i32 s1, s10, -2
	s_lshr_b32 s0, s1, 1
	s_add_i32 s0, s0, 1
	s_cmp_lt_u32 s1, 14
	s_mov_b32 s1, 0
	s_cbranch_scc1 .LBB0_1662
	s_add_i32 s13, s11, 0
	s_and_b32 s12, s0, -8
	s_add_i32 s13, s13, 0x20040
	v_mov_b32_e32 v1, 5

; __device__ __forceinline__ int moe_tables(Frame& F) {
;     ...
;         for (int e = 0; e < 8; ++e) { seg[e] = s; const int c = (int)__hip_atomic_load(F.ctl + CW_CNT + 64 * e, RLX_AGENT); const int nt = (c + 255) >> 8; for (int i = 0; i < nt; ++i) tile_e[(s >> 8) + i] = e; s += nt << 8; }
.LBB0_1669:
	s_and_b32 s0, s3, 0xffffff00
	s_add_i32 s2, s0, s2
	s_add_i32 s0, 0, 0x20418
	v_mov_b32_e32 v1, s0
	v_mov_b32_e32 v2, s2
	ds_write_b32 v1, v2
	v_mov_b32_e32 v1, 0x8000
	s_waitcnt vmcnt(0)
	v_mov_b32_e32 v2, v254
	s_nop 0
	v_readfirstlane_b32 s3, v2
	s_addk_i32 s3, 0xff
	s_ashr_i32 s10, s3, 8
	s_cmp_lt_i32 s10, 1
	s_cbranch_scc1 .LBB0_1681
	s_ashr_i32 s11, s2, 6
	s_cmp_eq_u32 s10, 1
	s_cbranch_scc1 .LBB0_1678
	s_add_i32 s1, s10, -2
	s_lshr_b32 s0, s1, 1
	s_add_i32 s0, s0, 1
	s_cmp_lt_u32 s1, 14
	s_mov_b32 s1, 0
	s_cbranch_scc1 .LBB0_1674
	s_add_i32 s13, s11, 0
	s_and_b32 s12, s0, -8
	s_add_i32 s13, s13, 0x20040
	v_mov_b32_e32 v2, 6

; __device__ __forceinline__ int moe_tables(Frame& F) {
;     ...
;         for (int e = 0; e < 8; ++e) { seg[e] = s; const int c = (int)__hip_atomic_load(F.ctl + CW_CNT + 64 * e, RLX_AGENT); const int nt = (c + 255) >> 8; for (int i = 0; i < nt; ++i) tile_e[(s >> 8) + i] = e; s += nt << 8; }
.LBB0_1681:
	s_and_b32 s0, s3, 0xffffff00
	s_add_i32 s2, s0, s2
	s_add_i32 s0, 0, 0x2041c
	v_mov_b32_e32 v2, s0
	v_mov_b32_e32 v3, s2
	ds_write_b32 v2, v3
	s_mov_b32 s12, 0
	s_waitcnt vmcnt(0)
	v_mov_b32_e32 v1, v255
	s_nop 0
	v_readfirstlane_b32 s3, v1
	s_addk_i32 s3, 0xff
	s_ashr_i32 s10, s3, 8
	s_cmp_lt_i32 s10, 1
	s_cbranch_scc1 .LBB0_1693
	s_ashr_i32 s11, s2, 6
	s_cmp_eq_u32 s10, 1
	s_mov_b64 s[0:1], -1
	s_cbranch_scc1 .LBB0_1690
	s_add_i32 s1, s10, -2
	s_lshr_b32 s0, s1, 1
	s_add_i32 s0, s0, 1
	s_cmp_lt_u32 s1, 14
	s_mov_b32 s1, 0
	s_cbranch_scc1 .LBB0_1686
	s_add_i32 s13, s11, 0
	s_and_b32 s12, s0, -8
	s_add_i32 s13, s13, 0x20040
	v_mov_b32_e32 v1, 7

; __device__ __forceinline__ void moe_gather(Frame& F) {
;     ...
;     for (int e = 0; e < 8; ++e) { const int c = (int)__hip_atomic_load(F.ctl + CW_CNT + 64 * e, RLX_AGENT);
;         for (int r = seg[e] + c + gw; r < seg[e + 1]; r += NGW) { v4u* dst = (v4u*)(AS + (size_t)r * DM) + F.lane;
; #pragma unroll
;             for (int j = 0; j < 2; ++j) dst[64 * j] = (v4u){0u, 0u, 0u, 0u}; } }
.LBB0_1701:
	v_mov_b32_e32 v1, 0x8000
	global_load_dword v248, v1, s[86:87] sc1
	global_load_dword v249, v1, s[86:87] offset:256 sc1
	global_load_dword v250, v1, s[86:87] offset:512 sc1
	global_load_dword v251, v1, s[86:87] offset:768 sc1
	global_load_dword v252, v1, s[86:87] offset:1024 sc1
	global_load_dword v253, v1, s[86:87] offset:1280 sc1
	global_load_dword v254, v1, s[86:87] offset:1536 sc1
	global_load_dword v255, v1, s[86:87] offset:1792 sc1
	s_add_i32 s0, 0, 0x20400
	v_mov_b32_e32 v2, s0
	ds_read_b64 v[2:3], v2
	s_waitcnt lgkmcnt(0)
	v_readfirstlane_b32 s0, v2
	v_readfirstlane_b32 s10, v3
	s_waitcnt vmcnt(0)
	v_mov_b32_e32 v4, v248
	s_nop 0
	v_readfirstlane_b32 s1, v4
	s_add_i32 s1, s1, s16
	s_add_i32 s0, s1, s0
	s_cmp_ge_i32 s0, s10
	s_cbranch_scc1 .LBB0_1704
	s_ashr_i32 s1, s0, 31
	s_lshl_b64 s[2:3], s[0:1], 11
	s_add_u32 s2, s86, s2
	s_mov_b32 s12, 0
	v_lshlrev_b32_e32 v2, 4, v186
	v_mov_b32_e32 v3, 0
	s_addc_u32 s3, s87, s3
	s_mov_b32 s13, s12
	v_lshl_add_u64 v[2:3], s[2:3], 0, v[2:3]
	s_mov_b64 s[2:3], 0x5f800000
	s_ashr_i32 s7, s6, 31
	s_mov_b32 s14, s12
	s_mov_b32 s15, s12
	v_mov_b64_e32 v[4:5], s[12:13]
	v_lshl_add_u64 v[2:3], v[2:3], 0, s[2:3]
	s_lshl_b64 s[2:3], s[6:7], 11
	v_mov_b64_e32 v[6:7], s[14:15]

; __device__ __forceinline__ void moe_gather(Frame& F) {
;     ...
;     for (int e = 0; e < 8; ++e) { const int c = (int)__hip_atomic_load(F.ctl + CW_CNT + 64 * e, RLX_AGENT);
;         for (int r = seg[e] + c + gw; r < seg[e + 1]; r += NGW) { v4u* dst = (v4u*)(AS + (size_t)r * DM) + F.lane;
; #pragma unroll
;             for (int j = 0; j < 2; ++j) dst[64 * j] = (v4u){0u, 0u, 0u, 0u}; } }
.LBB0_1704:
	s_add_i32 s0, 0, 0x20408
	v_mov_b32_e32 v2, s0
	ds_read_b32 v2, v2
	s_add_i32 s0, s10, s16
	s_waitcnt lgkmcnt(0)
	v_readfirstlane_b32 s14, v2
	s_waitcnt vmcnt(0)
	v_mov_b32_e32 v1, v249
	s_nop 0
	v_readfirstlane_b32 s1, v1
	s_add_i32 s10, s0, s1
	v_cmp_ge_i32_e32 vcc, s10, v2
	s_mov_b32 s0, 0
	s_cbranch_vccnz .LBB0_1707
	s_ashr_i32 s11, s10, 31
	s_lshl_b64 s[2:3], s[10:11], 11
	s_add_u32 s2, s86, s2
	v_lshlrev_b32_e32 v2, 4, v186
	v_mov_b32_e32 v3, 0
	s_addc_u32 s3, s87, s3
	v_lshl_add_u64 v[2:3], s[2:3], 0, v[2:3]
	s_mov_b64 s[2:3], 0x5f800000
	v_lshl_add_u64 v[2:3], v[2:3], 0, s[2:3]
	s_mov_b32 s2, s0
	s_mov_b32 s3, s0
	s_ashr_i32 s7, s6, 31
	s_mov_b32 s1, s0
	v_mov_b64_e32 v[6:7], s[2:3]
	s_lshl_b64 s[12:13], s[6:7], 11
	v_mov_b64_e32 v[4:5], s[0:1]

; __device__ __forceinline__ void moe_gather(Frame& F) {
;     ...
;     for (int e = 0; e < 8; ++e) { const int c = (int)__hip_atomic_load(F.ctl + CW_CNT + 64 * e, RLX_AGENT);
;         for (int r = seg[e] + c + gw; r < seg[e + 1]; r += NGW) { v4u* dst = (v4u*)(AS + (size_t)r * DM) + F.lane;
; #pragma unroll
;             for (int j = 0; j < 2; ++j) dst[64 * j] = (v4u){0u, 0u, 0u, 0u}; } }
.LBB0_1707:
	v_mov_b32_e32 v1, 0x8000
	s_add_i32 s0, 0, 0x2040c
	v_mov_b32_e32 v3, s0
	ds_read_b32 v3, v3
	s_add_i32 s0, s14, s16
	s_waitcnt lgkmcnt(0)
	v_readfirstlane_b32 s10, v3
	s_waitcnt vmcnt(0)
	v_mov_b32_e32 v2, v250
	s_nop 0
	v_readfirstlane_b32 s1, v2
	s_add_i32 s0, s0, s1
	v_cmp_ge_i32_e32 vcc, s0, v3
	s_cbranch_vccnz .LBB0_1710
	s_ashr_i32 s1, s0, 31
	s_lshl_b64 s[2:3], s[0:1], 11
	s_add_u32 s2, s86, s2
	s_mov_b32 s12, 0
	v_lshlrev_b32_e32 v2, 4, v186
	v_mov_b32_e32 v3, 0
	s_addc_u32 s3, s87, s3
	s_mov_b32 s13, s12
	v_lshl_add_u64 v[2:3], s[2:3], 0, v[2:3]
	s_mov_b64 s[2:3], 0x5f800000
	s_ashr_i32 s7, s6, 31
	s_mov_b32 s14, s12
	s_mov_b32 s15, s12
	v_mov_b64_e32 v[4:5], s[12:13]
	v_lshl_add_u64 v[2:3], v[2:3], 0, s[2:3]
	s_lshl_b64 s[2:3], s[6:7], 11
	v_mov_b64_e32 v[6:7], s[14:15]

; __device__ __forceinline__ void moe_gather(Frame& F) {
;     ...
;     for (int e = 0; e < 8; ++e) { const int c = (int)__hip_atomic_load(F.ctl + CW_CNT + 64 * e, RLX_AGENT);
;         for (int r = seg[e] + c + gw; r < seg[e + 1]; r += NGW) { v4u* dst = (v4u*)(AS + (size_t)r * DM) + F.lane;
; #pragma unroll
;             for (int j = 0; j < 2; ++j) dst[64 * j] = (v4u){0u, 0u, 0u, 0u}; } }
.LBB0_1710:
	s_add_i32 s0, 0, 0x20410
	v_mov_b32_e32 v2, s0
	ds_read_b32 v2, v2
	s_add_i32 s0, s10, s16
	s_waitcnt lgkmcnt(0)
	v_readfirstlane_b32 s14, v2
	s_waitcnt vmcnt(0)
	v_mov_b32_e32 v1, v251
	s_nop 0
	v_readfirstlane_b32 s1, v1
	s_add_i32 s10, s0, s1
	v_cmp_ge_i32_e32 vcc, s10, v2
	s_mov_b32 s0, 0
	s_cbranch_vccnz .LBB0_1713
	s_ashr_i32 s11, s10, 31
	s_lshl_b64 s[2:3], s[10:11], 11
	s_add_u32 s2, s86, s2
	v_lshlrev_b32_e32 v2, 4, v186
	v_mov_b32_e32 v3, 0
	s_addc_u32 s3, s87, s3
	v_lshl_add_u64 v[2:3], s[2:3], 0, v[2:3]
	s_mov_b64 s[2:3], 0x5f800000
	v_lshl_add_u64 v[2:3], v[2:3], 0, s[2:3]
	s_mov_b32 s2, s0
	s_mov_b32 s3, s0
	s_ashr_i32 s7, s6, 31
	s_mov_b32 s1, s0
	v_mov_b64_e32 v[6:7], s[2:3]
	s_lshl_b64 s[12:13], s[6:7], 11
	v_mov_b64_e32 v[4:5], s[0:1]

; __device__ __forceinline__ void moe_gather(Frame& F) {
;     ...
;     for (int e = 0; e < 8; ++e) { const int c = (int)__hip_atomic_load(F.ctl + CW_CNT + 64 * e, RLX_AGENT);
;         for (int r = seg[e] + c + gw; r < seg[e + 1]; r += NGW) { v4u* dst = (v4u*)(AS + (size_t)r * DM) + F.lane;
; #pragma unroll
;             for (int j = 0; j < 2; ++j) dst[64 * j] = (v4u){0u, 0u, 0u, 0u}; } }
.LBB0_1713:
	v_mov_b32_e32 v1, 0x8000
	s_add_i32 s0, 0, 0x20414
	v_mov_b32_e32 v3, s0
	ds_read_b32 v3, v3
	s_add_i32 s0, s14, s16
	s_waitcnt lgkmcnt(0)
	v_readfirstlane_b32 s10, v3
	s_waitcnt vmcnt(0)
	v_mov_b32_e32 v2, v252
	s_nop 0
	v_readfirstlane_b32 s1, v2
	s_add_i32 s0, s0, s1
	v_cmp_ge_i32_e32 vcc, s0, v3
	s_cbranch_vccnz .LBB0_1716
	s_ashr_i32 s1, s0, 31
	s_lshl_b64 s[2:3], s[0:1], 11
	s_add_u32 s2, s86, s2
	s_mov_b32 s12, 0
	v_lshlrev_b32_e32 v2, 4, v186
	v_mov_b32_e32 v3, 0
	s_addc_u32 s3, s87, s3
	s_mov_b32 s13, s12
	v_lshl_add_u64 v[2:3], s[2:3], 0, v[2:3]
	s_mov_b64 s[2:3], 0x5f800000
	s_ashr_i32 s7, s6, 31
	s_mov_b32 s14, s12
	s_mov_b32 s15, s12
	v_mov_b64_e32 v[4:5], s[12:13]
	v_lshl_add_u64 v[2:3], v[2:3], 0, s[2:3]
	s_lshl_b64 s[2:3], s[6:7], 11
	v_mov_b64_e32 v[6:7], s[14:15]

; __device__ __forceinline__ void moe_gather(Frame& F) {
;     ...
;     for (int e = 0; e < 8; ++e) { const int c = (int)__hip_atomic_load(F.ctl + CW_CNT + 64 * e, RLX_AGENT);
;         for (int r = seg[e] + c + gw; r < seg[e + 1]; r += NGW) { v4u* dst = (v4u*)(AS + (size_t)r * DM) + F.lane;
; #pragma unroll
;             for (int j = 0; j < 2; ++j) dst[64 * j] = (v4u){0u, 0u, 0u, 0u}; } }
.LBB0_1716:
	s_add_i32 s0, 0, 0x20418
	v_mov_b32_e32 v2, s0
	ds_read_b32 v2, v2
	s_add_i32 s0, s10, s16
	s_waitcnt lgkmcnt(0)
	v_readfirstlane_b32 s14, v2
	s_waitcnt vmcnt(0)
	v_mov_b32_e32 v1, v253
	s_nop 0
	v_readfirstlane_b32 s1, v1
	s_add_i32 s10, s0, s1
	v_cmp_ge_i32_e32 vcc, s10, v2
	s_mov_b32 s0, 0
	s_cbranch_vccnz .LBB0_1719
	s_ashr_i32 s11, s10, 31
	s_lshl_b64 s[2:3], s[10:11], 11
	s_add_u32 s2, s86, s2
	v_lshlrev_b32_e32 v2, 4, v186
	v_mov_b32_e32 v3, 0
	s_addc_u32 s3, s87, s3
	v_lshl_add_u64 v[2:3], s[2:3], 0, v[2:3]
	s_mov_b64 s[2:3], 0x5f800000
	v_lshl_add_u64 v[2:3], v[2:3], 0, s[2:3]
	s_mov_b32 s2, s0
	s_mov_b32 s3, s0
	s_ashr_i32 s7, s6, 31
	s_mov_b32 s1, s0
	v_mov_b64_e32 v[6:7], s[2:3]
	s_lshl_b64 s[12:13], s[6:7], 11
	v_mov_b64_e32 v[4:5], s[0:1]

; __device__ __forceinline__ void moe_gather(Frame& F) {
;     ...
;     for (int e = 0; e < 8; ++e) { const int c = (int)__hip_atomic_load(F.ctl + CW_CNT + 64 * e, RLX_AGENT);
;         for (int r = seg[e] + c + gw; r < seg[e + 1]; r += NGW) { v4u* dst = (v4u*)(AS + (size_t)r * DM) + F.lane;
; #pragma unroll
;             for (int j = 0; j < 2; ++j) dst[64 * j] = (v4u){0u, 0u, 0u, 0u}; } }
.LBB0_1719:
	v_mov_b32_e32 v1, 0x8000
	s_add_i32 s0, 0, 0x2041c
	v_mov_b32_e32 v3, s0
	ds_read_b32 v3, v3
	s_add_i32 s0, s14, s16
	s_waitcnt lgkmcnt(0)
	v_readfirstlane_b32 s10, v3
	s_waitcnt vmcnt(0)
	v_mov_b32_e32 v2, v254
	s_nop 0
	v_readfirstlane_b32 s1, v2
	s_add_i32 s0, s0, s1
	v_cmp_ge_i32_e32 vcc, s0, v3
	s_cbranch_vccnz .LBB0_1722
	s_ashr_i32 s1, s0, 31
	s_lshl_b64 s[2:3], s[0:1], 11
	s_add_u32 s2, s86, s2
	s_mov_b32 s12, 0
	v_lshlrev_b32_e32 v2, 4, v186
	v_mov_b32_e32 v3, 0
	s_addc_u32 s3, s87, s3
	s_mov_b32 s13, s12
	v_lshl_add_u64 v[2:3], s[2:3], 0, v[2:3]
	s_mov_b64 s[2:3], 0x5f800000
	s_ashr_i32 s7, s6, 31
	s_mov_b32 s14, s12
	s_mov_b32 s15, s12
	v_mov_b64_e32 v[4:5], s[12:13]
	v_lshl_add_u64 v[2:3], v[2:3], 0, s[2:3]
	s_lshl_b64 s[2:3], s[6:7], 11
	v_mov_b64_e32 v[6:7], s[14:15]

; __device__ __forceinline__ void moe_gather(Frame& F) {
;     ...
;     for (int e = 0; e < 8; ++e) { const int c = (int)__hip_atomic_load(F.ctl + CW_CNT + 64 * e, RLX_AGENT);
;         for (int r = seg[e] + c + gw; r < seg[e + 1]; r += NGW) { v4u* dst = (v4u*)(AS + (size_t)r * DM) + F.lane;
; #pragma unroll
;             for (int j = 0; j < 2; ++j) dst[64 * j] = (v4u){0u, 0u, 0u, 0u}; } }
.LBB0_1722:
	s_add_i32 s0, 0, 0x20420
	v_mov_b32_e32 v1, s0
	ds_read_b32 v1, v1
	s_add_i32 s0, s10, s16
	s_waitcnt vmcnt(0)
	v_mov_b32_e32 v2, v255
	s_nop 0
	v_readfirstlane_b32 s1, v2
	s_add_i32 s10, s0, s1
	s_waitcnt lgkmcnt(0)
	v_cmp_ge_i32_e32 vcc, s10, v1
	s_mov_b32 s0, 0
	s_cbranch_vccnz .LBB0_1725
	s_ashr_i32 s11, s10, 31
	s_lshl_b64 s[2:3], s[10:11], 11
	s_add_u32 s2, s86, s2
	v_lshlrev_b32_e32 v2, 4, v186
	v_mov_b32_e32 v3, 0
	s_addc_u32 s3, s87, s3
	v_lshl_add_u64 v[2:3], s[2:3], 0, v[2:3]
	s_mov_b64 s[2:3], 0x5f800000
	v_lshl_add_u64 v[2:3], v[2:3], 0, s[2:3]
	s_mov_b32 s2, s0
	s_mov_b32 s3, s0
	s_ashr_i32 s7, s6, 31
	s_mov_b32 s1, s0
	v_mov_b64_e32 v[6:7], s[2:3]
	s_lshl_b64 s[12:13], s[6:7], 11
	v_mov_b64_e32 v[4:5], s[0:1]

; #define LAS __attribute__((address_space(3)))
; __device__ __forceinline__ int moe_tables(Frame& F) {
;     LAS int* seg = (LAS int*)(F.lds + MISC_OFF + 1024); LAS int* tile_e = (LAS int*)(F.lds + MISC_OFF + 64);
;     if (F.tid == 0) { int s = 0;
;         for (int e = 0; e < 8; ++e) { seg[e] = s; const int c = (int)__hip_atomic_load(F.ctl + CW_CNT + 64 * e, RLX_AGENT); const int nt = (c + 255) >> 8; for (int i = 0; i < nt; ++i) tile_e[(s >> 8) + i] = e; s += nt << 8; }
;         seg[8] = s; }
.LBB0_1775:
	s_cmp_lt_i32 s68, 17
	s_cselect_b64 s[2:3], -1, 0
	s_and_b64 s[4:5], s[2:3], s[0:1]
	s_andn2_b64 vcc, exec, s[4:5]
	s_cbranch_vccnz .LBB0_1890
	v_cmp_eq_u32_e32 vcc, 0, v0
	s_and_saveexec_b64 s[6:7], vcc
	s_cbranch_execz .LBB0_1874
	s_add_i32 s0, 0, 0x20400
	v_mov_b32_e32 v1, 0
	s_waitcnt vmcnt(0)
	v_mov_b32_e32 v2, s0
	ds_write_b32 v2, v1
	v_mov_b32_e32 v1, 0x8000
	global_load_dword v248, v1, s[86:87] sc1
	global_load_dword v249, v1, s[86:87] offset:256 sc1
	global_load_dword v250, v1, s[86:87] offset:512 sc1
	global_load_dword v251, v1, s[86:87] offset:768 sc1
	global_load_dword v252, v1, s[86:87] offset:1024 sc1
	global_load_dword v253, v1, s[86:87] offset:1280 sc1
	global_load_dword v254, v1, s[86:87] offset:1536 sc1
	global_load_dword v255, v1, s[86:87] offset:1792 sc1
	s_waitcnt vmcnt(0)
	v_mov_b32_e32 v2, v248
	s_nop 0
	v_readfirstlane_b32 s10, v2
	s_addk_i32 s10, 0xff
	s_ashr_i32 s11, s10, 8
	s_cmp_lt_i32 s11, 1
	s_cbranch_scc1 .LBB0_1789
	s_cmp_lt_u32 s11, 4
	s_cbranch_scc1 .LBB0_1786
	s_add_i32 s0, s11, -4
	s_lshr_b32 s12, s0, 2
	s_add_i32 s12, s12, 1
	s_cmp_lt_u32 s0, 28
	s_mov_b32 s0, 0
	s_cbranch_scc1 .LBB0_1782
	s_mov_b32 s2, s0
	s_mov_b32 s3, s0
	s_mov_b32 s1, s0
	v_mov_b64_e32 v[4:5], s[2:3]
	s_add_i32 s13, 0, 0x20040
	s_and_b32 s14, s12, 0x7ffffff8
	v_mov_b64_e32 v[2:3], s[0:1]

; #define LAS __attribute__((address_space(3)))
; __device__ __forceinline__ int moe_tables(Frame& F) {
;     LAS int* seg = (LAS int*)(F.lds + MISC_OFF + 1024); LAS int* tile_e = (LAS int*)(F.lds + MISC_OFF + 64);
;     if (F.tid == 0) { int s = 0;
;         for (int e = 0; e < 8; ++e) { seg[e] = s; const int c = (int)__hip_atomic_load(F.ctl + CW_CNT + 64 * e, RLX_AGENT); const int nt = (c + 255) >> 8; for (int i = 0; i < nt; ++i) tile_e[(s >> 8) + i] = e; s += nt << 8; }
;         seg[8] = s; }
.LBB0_1940:
	s_cmp_lt_i32 s68, 18
	s_cselect_b64 s[2:3], -1, 0
	s_and_b64 s[10:11], s[2:3], s[0:1]
	s_andn2_b64 vcc, exec, s[10:11]
	s_cbranch_vccnz .LBB0_2140
	v_cmp_eq_u32_e64 s[0:1], 0, v0
	s_and_saveexec_b64 s[2:3], s[0:1]
	s_cbranch_execz .LBB0_2039
	s_add_i32 s4, 0, 0x20400
	v_mov_b32_e32 v1, 0
	s_waitcnt vmcnt(0)
	v_mov_b32_e32 v2, s4
	ds_write_b32 v2, v1
	v_mov_b32_e32 v1, 0x8000
	global_load_dword v248, v1, s[86:87] sc1
	global_load_dword v249, v1, s[86:87] offset:256 sc1
	global_load_dword v250, v1, s[86:87] offset:512 sc1
	global_load_dword v251, v1, s[86:87] offset:768 sc1
	global_load_dword v252, v1, s[86:87] offset:1024 sc1
	global_load_dword v253, v1, s[86:87] offset:1280 sc1
	global_load_dword v254, v1, s[86:87] offset:1536 sc1
	global_load_dword v255, v1, s[86:87] offset:1792 sc1
	s_waitcnt vmcnt(0)
	v_mov_b32_e32 v2, v248
	s_nop 0
	v_readfirstlane_b32 s12, v2
	s_addk_i32 s12, 0xff
	s_ashr_i32 s13, s12, 8
	s_cmp_lt_i32 s13, 1
	s_cbranch_scc1 .LBB0_1954
	s_cmp_lt_u32 s13, 4
	s_cbranch_scc1 .LBB0_1951
	s_add_i32 s4, s13, -4
	s_lshr_b32 s14, s4, 2
	s_add_i32 s14, s14, 1
	s_cmp_lt_u32 s4, 28
	s_mov_b32 s4, 0
	s_cbranch_scc1 .LBB0_1947
	s_mov_b32 s5, s4
	s_mov_b32 s6, s4
	s_mov_b32 s7, s4
	v_mov_b64_e32 v[2:3], s[4:5]
	s_add_i32 s15, 0, 0x20040
	s_and_b32 s16, s14, 0x7ffffff8
	v_mov_b64_e32 v[4:5], s[6:7]

; __device__ __forceinline__ int moe_tables(Frame& F) {
;     ...
;         for (int e = 0; e < 8; ++e) { seg[e] = s; const int c = (int)__hip_atomic_load(F.ctl + CW_CNT + 64 * e, RLX_AGENT); const int nt = (c + 255) >> 8; for (int i = 0; i < nt; ++i) tile_e[(s >> 8) + i] = e; s += nt << 8; }
.LBB0_1954:
	s_and_b32 s6, s12, 0xffffff00
	s_add_i32 s4, 0, 0x20404
	v_mov_b32_e32 v2, s4
	v_mov_b32_e32 v3, s6
	ds_write_b32 v2, v3
	s_mov_b32 s14, 0
	s_waitcnt vmcnt(0)
	v_mov_b32_e32 v1, v249
	s_nop 0
	v_readfirstlane_b32 s7, v1
	s_addk_i32 s7, 0xff
	s_ashr_i32 s12, s7, 8
	s_cmp_lt_i32 s12, 1
	s_cbranch_scc1 .LBB0_1966
	s_ashr_i32 s13, s6, 6
	s_cmp_eq_u32 s12, 1
	s_mov_b64 s[4:5], -1
	s_cbranch_scc1 .LBB0_1963
	s_add_i32 s5, s12, -2
	s_lshr_b32 s4, s5, 1
	s_add_i32 s4, s4, 1
	s_cmp_lt_u32 s5, 14
	s_mov_b32 s5, 0
	s_cbranch_scc1 .LBB0_1959
	s_add_i32 s15, s13, 0
	s_and_b32 s14, s4, -8
	s_add_i32 s15, s15, 0x20040
	v_mov_b32_e32 v1, 1

; __device__ __forceinline__ int moe_tables(Frame& F) {
;     ...
;         for (int e = 0; e < 8; ++e) { seg[e] = s; const int c = (int)__hip_atomic_load(F.ctl + CW_CNT + 64 * e, RLX_AGENT); const int nt = (c + 255) >> 8; for (int i = 0; i < nt; ++i) tile_e[(s >> 8) + i] = e; s += nt << 8; }
.LBB0_1966:
	s_and_b32 s4, s7, 0xffffff00
	s_add_i32 s6, s4, s6
	s_add_i32 s4, 0, 0x20408
	v_mov_b32_e32 v1, s4
	v_mov_b32_e32 v2, s6
	ds_write_b32 v1, v2
	v_mov_b32_e32 v1, 0x8000
	s_waitcnt vmcnt(0)
	v_mov_b32_e32 v2, v250
	s_nop 0
	v_readfirstlane_b32 s7, v2
	s_addk_i32 s7, 0xff
	s_ashr_i32 s12, s7, 8
	s_cmp_lt_i32 s12, 1
	s_cbranch_scc1 .LBB0_1978
	s_ashr_i32 s13, s6, 6
	s_cmp_eq_u32 s12, 1
	s_cbranch_scc1 .LBB0_1975
	s_add_i32 s5, s12, -2
	s_lshr_b32 s4, s5, 1
	s_add_i32 s4, s4, 1
	s_cmp_lt_u32 s5, 14
	s_mov_b32 s5, 0
	s_cbranch_scc1 .LBB0_1971
	s_add_i32 s15, s13, 0
	s_and_b32 s14, s4, -8
	s_add_i32 s15, s15, 0x20040
	v_mov_b32_e32 v2, 2

; __device__ __forceinline__ int moe_tables(Frame& F) {
;     ...
;         for (int e = 0; e < 8; ++e) { seg[e] = s; const int c = (int)__hip_atomic_load(F.ctl + CW_CNT + 64 * e, RLX_AGENT); const int nt = (c + 255) >> 8; for (int i = 0; i < nt; ++i) tile_e[(s >> 8) + i] = e; s += nt << 8; }
.LBB0_1978:
	s_and_b32 s4, s7, 0xffffff00
	s_add_i32 s6, s4, s6
	s_add_i32 s4, 0, 0x2040c
	v_mov_b32_e32 v2, s4
	v_mov_b32_e32 v3, s6
	ds_write_b32 v2, v3
	s_mov_b32 s14, 0
	s_waitcnt vmcnt(0)
	v_mov_b32_e32 v1, v251
	s_nop 0
	v_readfirstlane_b32 s7, v1
	s_addk_i32 s7, 0xff
	s_ashr_i32 s12, s7, 8
	s_cmp_lt_i32 s12, 1
	s_cbranch_scc1 .LBB0_1990
	s_ashr_i32 s13, s6, 6
	s_cmp_eq_u32 s12, 1
	s_mov_b64 s[4:5], -1
	s_cbranch_scc1 .LBB0_1987
	s_add_i32 s5, s12, -2
	s_lshr_b32 s4, s5, 1
	s_add_i32 s4, s4, 1
	s_cmp_lt_u32 s5, 14
	s_mov_b32 s5, 0
	s_cbranch_scc1 .LBB0_1983
	s_add_i32 s15, s13, 0
	s_and_b32 s14, s4, -8
	s_add_i32 s15, s15, 0x20040
	v_mov_b32_e32 v1, 3

; __device__ __forceinline__ int moe_tables(Frame& F) {
;     ...
;         for (int e = 0; e < 8; ++e) { seg[e] = s; const int c = (int)__hip_atomic_load(F.ctl + CW_CNT + 64 * e, RLX_AGENT); const int nt = (c + 255) >> 8; for (int i = 0; i < nt; ++i) tile_e[(s >> 8) + i] = e; s += nt << 8; }
.LBB0_1990:
	s_and_b32 s4, s7, 0xffffff00
	s_add_i32 s6, s4, s6
	s_add_i32 s4, 0, 0x20410
	v_mov_b32_e32 v1, s4
	v_mov_b32_e32 v2, s6
	ds_write_b32 v1, v2
	v_mov_b32_e32 v1, 0x8000
	s_waitcnt vmcnt(0)
	v_mov_b32_e32 v2, v252
	s_nop 0
	v_readfirstlane_b32 s7, v2
	s_addk_i32 s7, 0xff
	s_ashr_i32 s12, s7, 8
	s_cmp_lt_i32 s12, 1
	s_cbranch_scc1 .LBB0_2002
	s_ashr_i32 s13, s6, 6
	s_cmp_eq_u32 s12, 1
	s_cbranch_scc1 .LBB0_1999
	s_add_i32 s5, s12, -2
	s_lshr_b32 s4, s5, 1
	s_add_i32 s4, s4, 1
	s_cmp_lt_u32 s5, 14
	s_mov_b32 s5, 0
	s_cbranch_scc1 .LBB0_1995
	s_add_i32 s15, s13, 0
	s_and_b32 s14, s4, -8
	s_add_i32 s15, s15, 0x20040
	v_mov_b32_e32 v2, 4

; __device__ __forceinline__ int moe_tables(Frame& F) {
;     ...
;         for (int e = 0; e < 8; ++e) { seg[e] = s; const int c = (int)__hip_atomic_load(F.ctl + CW_CNT + 64 * e, RLX_AGENT); const int nt = (c + 255) >> 8; for (int i = 0; i < nt; ++i) tile_e[(s >> 8) + i] = e; s += nt << 8; }
.LBB0_2002:
	s_and_b32 s4, s7, 0xffffff00
	s_add_i32 s6, s4, s6
	s_add_i32 s4, 0, 0x20414
	v_mov_b32_e32 v2, s4
	v_mov_b32_e32 v3, s6
	ds_write_b32 v2, v3
	s_mov_b32 s14, 0
	s_waitcnt vmcnt(0)
	v_mov_b32_e32 v1, v253
	s_nop 0
	v_readfirstlane_b32 s7, v1
	s_addk_i32 s7, 0xff
	s_ashr_i32 s12, s7, 8
	s_cmp_lt_i32 s12, 1
	s_cbranch_scc1 .LBB0_2014
	s_ashr_i32 s13, s6, 6
	s_cmp_eq_u32 s12, 1
	s_mov_b64 s[4:5], -1
	s_cbranch_scc1 .LBB0_2011
	s_add_i32 s5, s12, -2
	s_lshr_b32 s4, s5, 1
	s_add_i32 s4, s4, 1
	s_cmp_lt_u32 s5, 14
	s_mov_b32 s5, 0
	s_cbranch_scc1 .LBB0_2007
	s_add_i32 s15, s13, 0
	s_and_b32 s14, s4, -8
	s_add_i32 s15, s15, 0x20040
	v_mov_b32_e32 v1, 5

; __device__ __forceinline__ int moe_tables(Frame& F) {
;     ...
;         for (int e = 0; e < 8; ++e) { seg[e] = s; const int c = (int)__hip_atomic_load(F.ctl + CW_CNT + 64 * e, RLX_AGENT); const int nt = (c + 255) >> 8; for (int i = 0; i < nt; ++i) tile_e[(s >> 8) + i] = e; s += nt << 8; }
.LBB0_2014:
	s_and_b32 s4, s7, 0xffffff00
	s_add_i32 s6, s4, s6
	s_add_i32 s4, 0, 0x20418
	v_mov_b32_e32 v1, s4
	v_mov_b32_e32 v2, s6
	ds_write_b32 v1, v2
	v_mov_b32_e32 v1, 0x8000
	s_waitcnt vmcnt(0)
	v_mov_b32_e32 v2, v254
	s_nop 0
	v_readfirstlane_b32 s7, v2
	s_addk_i32 s7, 0xff
	s_ashr_i32 s12, s7, 8
	s_cmp_lt_i32 s12, 1
	s_cbranch_scc1 .LBB0_2026
	s_ashr_i32 s13, s6, 6
	s_cmp_eq_u32 s12, 1
	s_cbranch_scc1 .LBB0_2023
	s_add_i32 s5, s12, -2
	s_lshr_b32 s4, s5, 1
	s_add_i32 s4, s4, 1
	s_cmp_lt_u32 s5, 14
	s_mov_b32 s5, 0
	s_cbranch_scc1 .LBB0_2019
	s_add_i32 s15, s13, 0
	s_and_b32 s14, s4, -8
	s_add_i32 s15, s15, 0x20040
	v_mov_b32_e32 v2, 6

; __device__ __forceinline__ int moe_tables(Frame& F) {
;     ...
;         for (int e = 0; e < 8; ++e) { seg[e] = s; const int c = (int)__hip_atomic_load(F.ctl + CW_CNT + 64 * e, RLX_AGENT); const int nt = (c + 255) >> 8; for (int i = 0; i < nt; ++i) tile_e[(s >> 8) + i] = e; s += nt << 8; }
.LBB0_2026:
	s_and_b32 s4, s7, 0xffffff00
	s_add_i32 s6, s4, s6
	s_add_i32 s4, 0, 0x2041c
	v_mov_b32_e32 v2, s4
	v_mov_b32_e32 v3, s6
	ds_write_b32 v2, v3
	s_mov_b32 s14, 0
	s_waitcnt vmcnt(0)
	v_mov_b32_e32 v1, v255
	s_nop 0
	v_readfirstlane_b32 s7, v1
	s_addk_i32 s7, 0xff
	s_ashr_i32 s12, s7, 8
	s_cmp_lt_i32 s12, 1
	s_cbranch_scc1 .LBB0_2038
	s_ashr_i32 s13, s6, 6
	s_cmp_eq_u32 s12, 1
	s_mov_b64 s[4:5], -1
	s_cbranch_scc1 .LBB0_2035
	s_add_i32 s5, s12, -2
	s_lshr_b32 s4, s5, 1
	s_add_i32 s4, s4, 1
	s_cmp_lt_u32 s5, 14
	s_mov_b32 s5, 0
	s_cbranch_scc1 .LBB0_2031
	s_add_i32 s15, s13, 0
	s_and_b32 s14, s4, -8
	s_add_i32 s15, s15, 0x20040
	v_mov_b32_e32 v1, 7

; __global__ void __launch_bounds__(NWAVES * 64, 2) hybrid_fwd(Args args) {
;     extern __shared__ __attribute__((aligned(16))) unsigned char lds[];
	.amdhsa_kernel _Z10hybrid_fwd4Args
		.amdhsa_group_segment_fixed_size 0
		.amdhsa_private_segment_fixed_size 0
		.amdhsa_kernarg_size 488
		.amdhsa_user_sgpr_count 2
		.amdhsa_user_sgpr_dispatch_ptr 0
		.amdhsa_user_sgpr_queue_ptr 0
		.amdhsa_user_sgpr_kernarg_segment_ptr 1
		.amdhsa_user_sgpr_dispatch_id 0
		.amdhsa_user_sgpr_kernarg_preload_length 0
		.amdhsa_user_sgpr_kernarg_preload_offset 0
		.amdhsa_user_sgpr_private_segment_size 0
		.amdhsa_uses_dynamic_stack 0
		.amdhsa_enable_private_segment 0
		.amdhsa_system_sgpr_workgroup_id_x 1
		.amdhsa_system_sgpr_workgroup_id_y 0
		.amdhsa_system_sgpr_workgroup_id_z 0
		.amdhsa_system_sgpr_workgroup_info 0
		.amdhsa_system_vgpr_workitem_id 0
		.amdhsa_next_free_vgpr 256
		.amdhsa_next_free_sgpr 102
		.amdhsa_accum_offset 256
		.amdhsa_reserve_vcc 1
		.amdhsa_float_round_mode_32 0
		.amdhsa_float_round_mode_16_64 0
		.amdhsa_float_denorm_mode_32 3
		.amdhsa_float_denorm_mode_16_64 3
		.amdhsa_dx10_clamp 1
		.amdhsa_ieee_mode 1
		.amdhsa_fp16_overflow 0
		.amdhsa_tg_split 0
		.amdhsa_exception_fp_ieee_invalid_op 0
		.amdhsa_exception_fp_denorm_src 0
		.amdhsa_exception_fp_ieee_div_zero 0
		.amdhsa_exception_fp_ieee_overflow 0
		.amdhsa_exception_fp_ieee_underflow 0
		.amdhsa_exception_fp_ieee_inexact 0
		.amdhsa_exception_int_div_zero 0
	.end_amdhsa_kernel

; __global__ void __launch_bounds__(NWAVES * 64, 2) hybrid_fwd(Args args) {
amdhsa.kernels:
  - .agpr_count:     0
    .args:
      - .offset:         0
        .size:           232
        .value_kind:     by_value
      - .offset:         232
        .size:           4
        .value_kind:     hidden_block_count_x
      - .offset:         236
        .size:           4
        .value_kind:     hidden_block_count_y
      - .offset:         240
        .size:           4
        .value_kind:     hidden_block_count_z
      - .offset:         244
        .size:           2
        .value_kind:     hidden_group_size_x
      - .offset:         246
        .size:           2
        .value_kind:     hidden_group_size_y
      - .offset:         248
        .size:           2
        .value_kind:     hidden_group_size_z
      - .offset:         250
        .size:           2
        .value_kind:     hidden_remainder_x
      - .offset:         252
        .size:           2
        .value_kind:     hidden_remainder_y
      - .offset:         254
        .size:           2
        .value_kind:     hidden_remainder_z
      - .offset:         272
        .size:           8
        .value_kind:     hidden_global_offset_x
      - .offset:         280
        .size:           8
        .value_kind:     hidden_global_offset_y
      - .offset:         288
        .size:           8
        .value_kind:     hidden_global_offset_z
      - .offset:         296
        .size:           2
        .value_kind:     hidden_grid_dims
      - .offset:         352
        .size:           4
        .value_kind:     hidden_dynamic_lds_size
    .group_segment_fixed_size: 0
    .kernarg_segment_align: 8
    .kernarg_segment_size: 488
    .language:       OpenCL C
    .language_version:
      - 2
      - 0
    .max_flat_workgroup_size: 512
    .name:           _Z10hybrid_fwd4Args
    .private_segment_fixed_size: 0
    .sgpr_count:     108
    .sgpr_spill_count: 148
    .symbol:         _Z10hybrid_fwd4Args.kd
    .uniform_work_group_size: 1
    .uses_dynamic_stack: false
    .vgpr_count:     256
    .vgpr_spill_count: 0
    .wavefront_size: 64
